# v18 plus rec gate math with scalar fma/mul/add instead of packed f32 ops
# speedup vs baseline: 1.0279x; 1.0279x over previous
.Lr0_gates:
	s_lshl_b32 s60, s58, 13
	s_mov_b32 s61, 0
	v_lshl_add_u64 v[196:197], v[196:197], 0, s[56:57]
	v_lshl_add_u64 v[198:199], v[198:199], 0, s[56:57]
	v_lshl_add_u64 v[200:201], v[200:201], 0, s[56:57]
	v_lshl_add_u64 v[202:203], v[202:203], 0, s[56:57]
	v_lshl_add_u64 v[204:205], v[108:109], 0, s[60:61]
	v_accvgpr_read_b32 v66, a8
	v_accvgpr_read_b32 v67, a9
	v_accvgpr_read_b32 v68, a10
	v_accvgpr_read_b32 v69, a11
	v_accvgpr_read_b32 v70, a12
	v_accvgpr_read_b32 v71, a13
	v_accvgpr_read_b32 v72, a14
	v_accvgpr_read_b32 v73, a15
	v_exp_f32_e32 v66, v66
	v_exp_f32_e32 v67, v67
	v_exp_f32_e32 v68, v68
	v_exp_f32_e32 v69, v69
	v_exp_f32_e32 v70, v70
	v_exp_f32_e32 v71, v71
	v_exp_f32_e32 v72, v72
	v_exp_f32_e32 v73, v73
	v_add_f32_e32 v66, 1.0, v66
	v_add_f32_e32 v67, 1.0, v67
	v_add_f32_e32 v68, 1.0, v68
	v_add_f32_e32 v69, 1.0, v69
	v_add_f32_e32 v70, 1.0, v70
	v_add_f32_e32 v71, 1.0, v71
	v_add_f32_e32 v72, 1.0, v72
	v_add_f32_e32 v73, 1.0, v73
	v_rcp_f32_e32 v70, v70
	v_rcp_f32_e32 v71, v71
	v_rcp_f32_e32 v72, v72
	v_rcp_f32_e32 v73, v73
	v_rcp_f32_e32 v74, v66
	v_rcp_f32_e32 v75, v67
	v_rcp_f32_e32 v76, v68
	v_rcp_f32_e32 v77, v69
	v_fma_f32 v70, v100, v70, v102
	v_fma_f32 v71, v100, v71, v102
	v_fma_f32 v72, v100, v72, v102
	v_fma_f32 v73, v100, v73, v102
	v_mul_f32_e32 v78, v74, v70
	v_mul_f32_e32 v79, v75, v71
	v_mul_f32_e32 v80, v76, v72
	v_mul_f32_e32 v81, v77, v73
	v_mov_b32_e32 v82, v78
	v_mov_b32_e32 v83, v79
	v_mov_b32_e32 v84, v80
	v_mov_b32_e32 v85, v81
	v_permlane32_swap_b32_e32 v78, v82
	v_permlane32_swap_b32_e32 v79, v83
	v_permlane32_swap_b32_e32 v80, v84
	v_permlane32_swap_b32_e32 v81, v85
	v_fma_f32 v112, v112, v74, v78
	v_fma_f32 v113, v113, v75, v79
	v_fma_f32 v110, v110, v76, v80
	v_fma_f32 v111, v111, v77, v81
	v_exp_f32_e32 v86, v112
	v_exp_f32_e32 v87, v113
	v_exp_f32_e32 v88, v110
	v_exp_f32_e32 v89, v111
	v_add_f32_e32 v86, 1.0, v86
	v_add_f32_e32 v87, 1.0, v87
	v_add_f32_e32 v88, 1.0, v88
	v_add_f32_e32 v89, 1.0, v89
	v_rcp_f32_e32 v86, v86
	v_rcp_f32_e32 v87, v87
	v_rcp_f32_e32 v88, v88
	v_rcp_f32_e32 v89, v89
	v_fma_f32 v86, v86, -2.0, 1.0
	v_fma_f32 v87, v87, -2.0, 1.0
	v_fma_f32 v88, v88, -2.0, 1.0
	v_fma_f32 v89, v89, -2.0, 1.0
	v_mul_f32_e32 v66, v70, v86
	v_mul_f32_e32 v67, v71, v87
	v_mul_f32_e32 v68, v72, v88
	v_mul_f32_e32 v69, v73, v89
	v_cvt_pk_f16_f32 v90, v66, v67
	v_cvt_pk_f16_f32 v91, v68, v69
	v_lshl_add_u32 v93, s54, 8, v99
	s_and_saveexec_b64 s[62:63], s[6:7]
	global_store_dwordx2 v[204:205], v[90:91], off
	ds_write_b64 v93, v[90:91] offset:61440
	s_or_b64 exec, exec, s[62:63]
	s_cmp_eq_u32 s54, 29
	s_cbranch_scc1 .Lr0_noissue
	global_load_dwordx4 v[132:135], v[196:197], off nt
	global_load_dwordx4 v[136:139], v[196:197], off offset:1024 nt
	global_load_dwordx4 v[140:143], v[196:197], off offset:2048 nt
	global_load_dwordx4 v[144:147], v[196:197], off offset:3072 nt
	global_load_dwordx4 v[148:151], v[198:199], off nt
	global_load_dwordx4 v[152:155], v[198:199], off offset:1024 nt
	global_load_dwordx4 v[156:159], v[198:199], off offset:2048 nt
	global_load_dwordx4 v[160:163], v[198:199], off offset:3072 nt

.Lr1_gates:
	s_lshl_b32 s60, s58, 13
	s_mov_b32 s61, 0
	v_lshl_add_u64 v[196:197], v[196:197], 0, s[56:57]
	v_lshl_add_u64 v[198:199], v[198:199], 0, s[56:57]
	v_lshl_add_u64 v[200:201], v[200:201], 0, s[56:57]
	v_lshl_add_u64 v[202:203], v[202:203], 0, s[56:57]
	v_lshl_add_u64 v[204:205], v[112:113], 0, s[60:61]
	ds_read_b32 v92, v107 offset:61576
	v_accvgpr_read_b32 v66, a8
	v_accvgpr_read_b32 v67, a9
	v_accvgpr_read_b32 v68, a10
	v_accvgpr_read_b32 v69, a11
	v_accvgpr_read_b32 v70, a12
	v_accvgpr_read_b32 v71, a13
	v_accvgpr_read_b32 v72, a14
	v_accvgpr_read_b32 v73, a15
	v_exp_f32_e32 v66, v66
	v_exp_f32_e32 v67, v67
	v_exp_f32_e32 v68, v68
	v_exp_f32_e32 v69, v69
	v_exp_f32_e32 v70, v70
	v_exp_f32_e32 v71, v71
	v_exp_f32_e32 v72, v72
	v_exp_f32_e32 v73, v73
	v_add_f32_e32 v66, 1.0, v66
	v_add_f32_e32 v67, 1.0, v67
	v_add_f32_e32 v68, 1.0, v68
	v_add_f32_e32 v69, 1.0, v69
	v_add_f32_e32 v70, 1.0, v70
	v_add_f32_e32 v71, 1.0, v71
	v_add_f32_e32 v72, 1.0, v72
	v_add_f32_e32 v73, 1.0, v73
	v_rcp_f32_e32 v70, v70
	v_rcp_f32_e32 v71, v71
	v_rcp_f32_e32 v72, v72
	v_rcp_f32_e32 v73, v73
	v_rcp_f32_e32 v74, v66
	v_rcp_f32_e32 v75, v67
	v_rcp_f32_e32 v76, v68
	v_rcp_f32_e32 v77, v69
	v_fma_f32 v70, v100, v70, v102
	v_fma_f32 v71, v100, v71, v102
	v_fma_f32 v72, v100, v72, v102
	v_fma_f32 v73, v100, v73, v102
	v_mul_f32_e32 v78, v74, v70
	v_mul_f32_e32 v79, v75, v71
	v_mul_f32_e32 v80, v76, v72
	v_mul_f32_e32 v81, v77, v73
	v_mov_b32_e32 v82, v78
	v_mov_b32_e32 v83, v79
	v_mov_b32_e32 v84, v80
	v_mov_b32_e32 v85, v81
	v_permlane32_swap_b32_e32 v78, v82
	v_permlane32_swap_b32_e32 v79, v83
	v_permlane32_swap_b32_e32 v80, v84
	v_permlane32_swap_b32_e32 v81, v85
	v_fma_f32 v116, v116, v74, v78
	v_fma_f32 v117, v117, v75, v79
	v_fma_f32 v114, v114, v76, v80
	v_fma_f32 v115, v115, v77, v81
	v_exp_f32_e32 v86, v116
	v_exp_f32_e32 v87, v117
	v_exp_f32_e32 v88, v114
	v_exp_f32_e32 v89, v115
	v_add_f32_e32 v86, 1.0, v86
	v_add_f32_e32 v87, 1.0, v87
	v_add_f32_e32 v88, 1.0, v88
	v_add_f32_e32 v89, 1.0, v89
	v_rcp_f32_e32 v86, v86
	v_rcp_f32_e32 v87, v87
	v_rcp_f32_e32 v88, v88
	v_rcp_f32_e32 v89, v89
	v_fma_f32 v86, v86, -2.0, 1.0
	v_fma_f32 v87, v87, -2.0, 1.0
	v_fma_f32 v88, v88, -2.0, 1.0
	v_fma_f32 v89, v89, -2.0, 1.0
	v_mul_f32_e32 v66, v70, v86
	v_mul_f32_e32 v67, v71, v87
	v_mul_f32_e32 v68, v72, v88
	v_mul_f32_e32 v69, v73, v89
	v_cvt_pk_f16_f32 v90, v66, v67
	v_cvt_pk_f16_f32 v91, v68, v69
	v_lshl_add_u32 v93, s54, 8, v99
	s_waitcnt lgkmcnt(0)
	v_cmp_lt_i32_e32 vcc, s54, v92
	s_cbranch_vccnz .Lr1_pubok

.Lr1_noissue:
	s_add_i32 s54, s54, 1
	s_add_i32 s60, s54, 30
	v_mov_b32_e32 v94, s60
	ds_write_b32 v107, v94 offset:61572
	ds_write_b32 v107, v94 offset:61568
	v_add_f32_e32 v108, v108, v66
	v_add_f32_e32 v110, v110, v68
	v_add_f32_e32 v109, v109, v67
	v_add_f32_e32 v111, v111, v69
	s_sub_i32 s58, s58, s44
	s_cmp_lg_u32 s54, 30
	s_cbranch_scc1 .Lr1_top
	s_waitcnt vmcnt(0)
